# speedup vs baseline: 1.0036x; 1.0036x over previous
.LBB1_9:
	ds_read_b128 v[130:133], v191
	ds_read_b128 v[134:137], v191 offset:1024
	ds_read_b128 v[138:141], v191 offset:2048
	ds_read_b128 v[142:145], v191 offset:3072
	ds_read_b128 v[146:149], v192
	ds_read_b128 v[150:153], v192 offset:1024
	ds_read_b128 v[154:157], v192 offset:2048
	ds_read_b128 v[158:161], v192 offset:3072
	s_add_u32 s8, s6, 0xfff80080
	s_addc_u32 s9, s7, -1
	s_cmp_eq_u32 s56, 28
	s_cselect_b32 s53, s5, s9
	s_cselect_b32 s52, s10, s8
	s_cselect_b32 s9, s27, s55
	s_cselect_b32 s8, s37, s54
	v_lshl_add_u64 v[184:185], s[6:7], 0, v[176:177]
	s_add_i32 m0, s58, 0xc000
	ds_read_b128 v[200:203], v193
	ds_read_b128 v[204:207], v193 offset:1024
	ds_read_b128 v[208:211], v193 offset:2048
	ds_read_b128 v[212:215], v193 offset:3072
	ds_read_b128 v[216:219], v193 offset:4096
	ds_read_b128 v[220:223], v193 offset:5120
	ds_read_b128 v[224:227], v193 offset:6144
	ds_read_b128 v[228:231], v193 offset:7168
	global_load_lds_dwordx4 v[184:185], off
	v_lshl_add_u64 v[184:185], s[6:7], 0, v[178:179]
	s_add_i32 m0, s58, 0xe000
	s_nop 0
	global_load_lds_dwordx4 v[184:185], off
	s_cmp_lt_i32 s56, 14
	s_cbranch_scc1 .Lqkv_nopoll
	s_cmp_gt_i32 s56, 24
	s_cbranch_scc1 .Lqkv_nopoll
	s_bitcmp1_b32 s56, 1
	s_cbranch_scc0 .Lqkv_chk
	s_sub_u32 s82, s56, 14
	s_lshl_b32 s82, s82, 6
	v_add_u32_e32 v242, s82, v241
	global_load_dword v240, v242, s[80:81] sc1
	s_branch .Lqkv_nopoll

.Lqkv_nopoll:
	s_waitcnt vmcnt(8)
	s_waitcnt lgkmcnt(0)
	s_barrier
	s_setprio 1
	s_waitcnt lgkmcnt(0)
	v_mfma_f32_16x16x32_f16 v[126:129], v[130:133], v[200:203], v[126:129]
	v_mfma_f32_16x16x32_f16 v[122:125], v[138:141], v[200:203], v[122:125]
	v_mfma_f32_16x16x32_f16 v[118:121], v[130:133], v[208:211], v[118:121]
	v_mfma_f32_16x16x32_f16 v[114:117], v[138:141], v[208:211], v[114:117]
	v_mfma_f32_16x16x32_f16 v[102:105], v[130:133], v[216:219], v[102:105]
	v_mfma_f32_16x16x32_f16 v[98:101], v[138:141], v[216:219], v[98:101]
	v_mfma_f32_16x16x32_f16 v[86:89], v[130:133], v[224:227], v[86:89]
	v_mfma_f32_16x16x32_f16 v[82:85], v[138:141], v[224:227], v[82:85]
	v_mfma_f32_16x16x32_f16 v[126:129], v[134:137], v[204:207], v[126:129]
	v_mfma_f32_16x16x32_f16 v[122:125], v[142:145], v[204:207], v[122:125]
	v_mfma_f32_16x16x32_f16 v[118:121], v[134:137], v[212:215], v[118:121]
	v_mfma_f32_16x16x32_f16 v[114:117], v[142:145], v[212:215], v[114:117]
	v_mfma_f32_16x16x32_f16 v[102:105], v[134:137], v[220:223], v[102:105]
	v_mfma_f32_16x16x32_f16 v[98:101], v[142:145], v[220:223], v[98:101]
	v_mfma_f32_16x16x32_f16 v[86:89], v[134:137], v[228:231], v[86:89]
	v_mfma_f32_16x16x32_f16 v[82:85], v[142:145], v[228:231], v[82:85]
	s_setprio 0
	s_setprio 1
	v_mfma_f32_16x16x32_f16 v[110:113], v[146:149], v[200:203], v[110:113]
	v_mfma_f32_16x16x32_f16 v[106:109], v[154:157], v[200:203], v[106:109]
	v_mfma_f32_16x16x32_f16 v[94:97], v[146:149], v[208:211], v[94:97]
	v_mfma_f32_16x16x32_f16 v[90:93], v[154:157], v[208:211], v[90:93]
	v_mfma_f32_16x16x32_f16 v[78:81], v[146:149], v[216:219], v[78:81]
	v_mfma_f32_16x16x32_f16 v[74:77], v[154:157], v[216:219], v[74:77]
	v_mfma_f32_16x16x32_f16 v[70:73], v[146:149], v[224:227], v[70:73]
	v_mfma_f32_16x16x32_f16 v[66:69], v[154:157], v[224:227], v[66:69]
	v_mfma_f32_16x16x32_f16 v[110:113], v[150:153], v[204:207], v[110:113]
	v_mfma_f32_16x16x32_f16 v[106:109], v[158:161], v[204:207], v[106:109]
	v_mfma_f32_16x16x32_f16 v[94:97], v[150:153], v[212:215], v[94:97]
	v_mfma_f32_16x16x32_f16 v[90:93], v[158:161], v[212:215], v[90:93]
	v_mfma_f32_16x16x32_f16 v[78:81], v[150:153], v[220:223], v[78:81]
	v_mfma_f32_16x16x32_f16 v[74:77], v[158:161], v[220:223], v[74:77]
	v_mfma_f32_16x16x32_f16 v[70:73], v[150:153], v[228:231], v[70:73]
	v_mfma_f32_16x16x32_f16 v[66:69], v[158:161], v[228:231], v[66:69]
	s_setprio 0
	s_barrier
	s_add_i32 s57, s68, s3
	v_lshl_add_u64 v[184:185], s[8:9], 0, v[164:165]
	s_mov_b32 m0, s57
	ds_read_b128 v[200:203], v193 offset:16384
	ds_read_b128 v[204:207], v193 offset:17408
	ds_read_b128 v[208:211], v193 offset:18432
	ds_read_b128 v[212:215], v193 offset:19456
	ds_read_b128 v[216:219], v193 offset:20480
	ds_read_b128 v[220:223], v193 offset:21504
	ds_read_b128 v[224:227], v193 offset:22528
	ds_read_b128 v[228:231], v193 offset:23552
	global_load_lds_dwordx4 v[184:185], off
	s_add_i32 m0, s57, 0x2000
	s_add_u32 s78, s8, 0x20000
	v_lshl_add_u64 v[232:233], s[8:9], 0, v[168:169]
	s_addc_u32 s79, s9, 0
	s_add_i32 s57, s69, s3
	global_load_lds_dwordx4 v[232:233], off
	v_lshl_add_u64 v[234:235], s[78:79], 0, v[164:165]
	s_mov_b32 m0, s57
	v_lshl_add_u64 v[236:237], s[52:53], 0, v[166:167]
	global_load_lds_dwordx4 v[234:235], off
	v_lshl_add_u64 v[234:235], s[78:79], 0, v[168:169]
	s_add_i32 m0, s57, 0x2000
	s_nop 0
	global_load_lds_dwordx4 v[234:235], off
	v_lshl_add_u64 v[234:235], s[52:53], 0, v[162:163]
	s_mov_b32 m0, s58
	s_nop 0
	global_load_lds_dwordx4 v[234:235], off
	s_mov_b32 m0, s59
	s_nop 0
	global_load_lds_dwordx4 v[236:237], off
	s_waitcnt vmcnt(8)
	s_waitcnt lgkmcnt(0)
	s_barrier
	s_setprio 1
	s_waitcnt lgkmcnt(0)
	v_mfma_f32_16x16x32_f16 v[62:65], v[130:133], v[200:203], v[62:65]
	v_mfma_f32_16x16x32_f16 v[58:61], v[138:141], v[200:203], v[58:61]
	v_mfma_f32_16x16x32_f16 v[54:57], v[130:133], v[208:211], v[54:57]
	v_mfma_f32_16x16x32_f16 v[50:53], v[138:141], v[208:211], v[50:53]
	v_mfma_f32_16x16x32_f16 v[38:41], v[130:133], v[216:219], v[38:41]
	v_mfma_f32_16x16x32_f16 v[34:37], v[138:141], v[216:219], v[34:37]
	v_mfma_f32_16x16x32_f16 v[22:25], v[130:133], v[224:227], v[22:25]
	v_mfma_f32_16x16x32_f16 v[18:21], v[138:141], v[224:227], v[18:21]
	v_mfma_f32_16x16x32_f16 v[62:65], v[134:137], v[204:207], v[62:65]
	v_mfma_f32_16x16x32_f16 v[58:61], v[142:145], v[204:207], v[58:61]
	v_mfma_f32_16x16x32_f16 v[54:57], v[134:137], v[212:215], v[54:57]
	v_mfma_f32_16x16x32_f16 v[50:53], v[142:145], v[212:215], v[50:53]
	v_mfma_f32_16x16x32_f16 v[38:41], v[134:137], v[220:223], v[38:41]
	v_mfma_f32_16x16x32_f16 v[34:37], v[142:145], v[220:223], v[34:37]
	v_mfma_f32_16x16x32_f16 v[22:25], v[134:137], v[228:231], v[22:25]
	v_mfma_f32_16x16x32_f16 v[18:21], v[142:145], v[228:231], v[18:21]
	s_setprio 0
	s_setprio 1
	v_mfma_f32_16x16x32_f16 v[46:49], v[146:149], v[200:203], v[46:49]
	v_mfma_f32_16x16x32_f16 v[42:45], v[154:157], v[200:203], v[42:45]
	v_mfma_f32_16x16x32_f16 v[30:33], v[146:149], v[208:211], v[30:33]
	v_mfma_f32_16x16x32_f16 v[26:29], v[154:157], v[208:211], v[26:29]
	v_mfma_f32_16x16x32_f16 v[14:17], v[146:149], v[216:219], v[14:17]
	v_mfma_f32_16x16x32_f16 v[10:13], v[154:157], v[216:219], v[10:13]
	v_mfma_f32_16x16x32_f16 v[6:9], v[146:149], v[224:227], v[6:9]
	v_mfma_f32_16x16x32_f16 v[2:5], v[154:157], v[224:227], v[2:5]
	v_mfma_f32_16x16x32_f16 v[46:49], v[150:153], v[204:207], v[46:49]
	v_mfma_f32_16x16x32_f16 v[42:45], v[158:161], v[204:207], v[42:45]
	v_mfma_f32_16x16x32_f16 v[30:33], v[150:153], v[212:215], v[30:33]
	v_mfma_f32_16x16x32_f16 v[26:29], v[158:161], v[212:215], v[26:29]
	v_mfma_f32_16x16x32_f16 v[14:17], v[150:153], v[220:223], v[14:17]
	v_mfma_f32_16x16x32_f16 v[10:13], v[158:161], v[220:223], v[10:13]
	v_mfma_f32_16x16x32_f16 v[6:9], v[150:153], v[228:231], v[6:9]
	v_mfma_f32_16x16x32_f16 v[2:5], v[158:161], v[228:231], v[2:5]
	s_setprio 0
	s_barrier
	s_add_i32 s57, 0, 0x18000
	s_add_i32 s78, 0, 0x1c000
	v_add_u32_e32 v142, s57, v186
	v_add_u32_e32 v158, s78, v186
	ds_read_b128 v[130:133], v142
	ds_read_b128 v[134:137], v142 offset:1024
	ds_read_b128 v[138:141], v142 offset:2048
	ds_read_b128 v[142:145], v142 offset:3072
	ds_read_b128 v[146:149], v158
	ds_read_b128 v[150:153], v158 offset:1024
	ds_read_b128 v[154:157], v158 offset:2048
	ds_read_b128 v[158:161], v158 offset:3072
	s_add_u32 s52, s52, 0x80000
	s_addc_u32 s53, s53, 0
	s_mov_b32 m0, s60
	v_lshl_add_u64 v[238:239], s[52:53], 0, v[162:163]
	ds_read_b128 v[200:203], v193 offset:32768
	ds_read_b128 v[204:207], v193 offset:33792
	ds_read_b128 v[208:211], v193 offset:34816
	ds_read_b128 v[212:215], v193 offset:35840
	ds_read_b128 v[216:219], v193 offset:36864
	ds_read_b128 v[220:223], v193 offset:37888
	ds_read_b128 v[224:227], v193 offset:38912
	ds_read_b128 v[228:231], v193 offset:39936
	global_load_lds_dwordx4 v[238:239], off
	v_lshl_add_u64 v[238:239], s[52:53], 0, v[166:167]
	s_mov_b32 m0, s61
	s_nop 0
	global_load_lds_dwordx4 v[238:239], off
	s_waitcnt vmcnt(8)
	s_waitcnt lgkmcnt(0)
	s_barrier
	s_setprio 1
	s_waitcnt lgkmcnt(0)
	v_mfma_f32_16x16x32_f16 v[126:129], v[130:133], v[200:203], v[126:129]
	v_mfma_f32_16x16x32_f16 v[122:125], v[138:141], v[200:203], v[122:125]
	v_mfma_f32_16x16x32_f16 v[118:121], v[130:133], v[208:211], v[118:121]
	v_mfma_f32_16x16x32_f16 v[114:117], v[138:141], v[208:211], v[114:117]
	v_mfma_f32_16x16x32_f16 v[102:105], v[130:133], v[216:219], v[102:105]
	v_mfma_f32_16x16x32_f16 v[98:101], v[138:141], v[216:219], v[98:101]
	v_mfma_f32_16x16x32_f16 v[86:89], v[130:133], v[224:227], v[86:89]
	v_mfma_f32_16x16x32_f16 v[82:85], v[138:141], v[224:227], v[82:85]
	v_mfma_f32_16x16x32_f16 v[126:129], v[134:137], v[204:207], v[126:129]
	v_mfma_f32_16x16x32_f16 v[122:125], v[142:145], v[204:207], v[122:125]
	v_mfma_f32_16x16x32_f16 v[118:121], v[134:137], v[212:215], v[118:121]
	v_mfma_f32_16x16x32_f16 v[114:117], v[142:145], v[212:215], v[114:117]
	v_mfma_f32_16x16x32_f16 v[102:105], v[134:137], v[220:223], v[102:105]
	v_mfma_f32_16x16x32_f16 v[98:101], v[142:145], v[220:223], v[98:101]
	v_mfma_f32_16x16x32_f16 v[86:89], v[134:137], v[228:231], v[86:89]
	v_mfma_f32_16x16x32_f16 v[82:85], v[142:145], v[228:231], v[82:85]
	s_setprio 0
	s_setprio 1
	v_mfma_f32_16x16x32_f16 v[110:113], v[146:149], v[200:203], v[110:113]
	v_mfma_f32_16x16x32_f16 v[106:109], v[154:157], v[200:203], v[106:109]
	v_mfma_f32_16x16x32_f16 v[94:97], v[146:149], v[208:211], v[94:97]
	v_mfma_f32_16x16x32_f16 v[90:93], v[154:157], v[208:211], v[90:93]
	v_mfma_f32_16x16x32_f16 v[78:81], v[146:149], v[216:219], v[78:81]
	v_mfma_f32_16x16x32_f16 v[74:77], v[154:157], v[216:219], v[74:77]
	v_mfma_f32_16x16x32_f16 v[70:73], v[146:149], v[224:227], v[70:73]
	v_mfma_f32_16x16x32_f16 v[66:69], v[154:157], v[224:227], v[66:69]
	v_mfma_f32_16x16x32_f16 v[110:113], v[150:153], v[204:207], v[110:113]
	v_mfma_f32_16x16x32_f16 v[106:109], v[158:161], v[204:207], v[106:109]
	v_mfma_f32_16x16x32_f16 v[94:97], v[150:153], v[212:215], v[94:97]
	v_mfma_f32_16x16x32_f16 v[90:93], v[158:161], v[212:215], v[90:93]
	v_mfma_f32_16x16x32_f16 v[78:81], v[150:153], v[220:223], v[78:81]
	v_mfma_f32_16x16x32_f16 v[74:77], v[158:161], v[220:223], v[74:77]
	v_mfma_f32_16x16x32_f16 v[70:73], v[150:153], v[228:231], v[70:73]
	v_mfma_f32_16x16x32_f16 v[66:69], v[158:161], v[228:231], v[66:69]
	s_setprio 0
	s_barrier
	s_add_i32 s52, s57, s3
	v_lshl_add_u64 v[184:185], v[184:185], 0, s[44:45]
	s_mov_b32 m0, s52
	ds_read_b128 v[200:203], v193 offset:49152
	ds_read_b128 v[204:207], v193 offset:50176
	ds_read_b128 v[208:211], v193 offset:51200
	ds_read_b128 v[212:215], v193 offset:52224
	ds_read_b128 v[216:219], v193 offset:53248
	ds_read_b128 v[220:223], v193 offset:54272
	ds_read_b128 v[224:227], v193 offset:55296
	ds_read_b128 v[228:231], v193 offset:56320
	global_load_lds_dwordx4 v[184:185], off
	s_add_i32 m0, s52, 0x2000
	s_add_u32 s8, s8, 0x20080
	v_lshl_add_u64 v[184:185], v[232:233], 0, s[44:45]
	s_addc_u32 s9, s9, 0
	s_add_i32 s52, s78, s3
	global_load_lds_dwordx4 v[184:185], off
	v_lshl_add_u64 v[184:185], s[8:9], 0, v[164:165]
	s_mov_b32 m0, s52
	s_nop 0
	global_load_lds_dwordx4 v[184:185], off
	v_lshl_add_u64 v[184:185], s[8:9], 0, v[168:169]
	s_add_i32 m0, s52, 0x2000
	s_nop 0
	global_load_lds_dwordx4 v[184:185], off
	v_lshl_add_u64 v[184:185], v[234:235], 0, s[44:45]
	s_mov_b32 m0, s64
	s_nop 0
	global_load_lds_dwordx4 v[184:185], off
	v_lshl_add_u64 v[184:185], v[236:237], 0, s[44:45]
	s_mov_b32 m0, s65
	s_nop 0
	global_load_lds_dwordx4 v[184:185], off
	s_waitcnt vmcnt(8)
	s_waitcnt lgkmcnt(0)
	s_barrier
	s_setprio 1
	s_waitcnt lgkmcnt(0)
	v_mfma_f32_16x16x32_f16 v[62:65], v[130:133], v[200:203], v[62:65]
	v_mfma_f32_16x16x32_f16 v[58:61], v[138:141], v[200:203], v[58:61]
	v_mfma_f32_16x16x32_f16 v[54:57], v[130:133], v[208:211], v[54:57]
	v_mfma_f32_16x16x32_f16 v[50:53], v[138:141], v[208:211], v[50:53]
	v_mfma_f32_16x16x32_f16 v[38:41], v[130:133], v[216:219], v[38:41]
	v_mfma_f32_16x16x32_f16 v[34:37], v[138:141], v[216:219], v[34:37]
	v_mfma_f32_16x16x32_f16 v[22:25], v[130:133], v[224:227], v[22:25]
	v_mfma_f32_16x16x32_f16 v[18:21], v[138:141], v[224:227], v[18:21]
	v_mfma_f32_16x16x32_f16 v[62:65], v[134:137], v[204:207], v[62:65]
	v_mfma_f32_16x16x32_f16 v[58:61], v[142:145], v[204:207], v[58:61]
	v_mfma_f32_16x16x32_f16 v[54:57], v[134:137], v[212:215], v[54:57]
	v_mfma_f32_16x16x32_f16 v[50:53], v[142:145], v[212:215], v[50:53]
	v_mfma_f32_16x16x32_f16 v[38:41], v[134:137], v[220:223], v[38:41]
	v_mfma_f32_16x16x32_f16 v[34:37], v[142:145], v[220:223], v[34:37]
	v_mfma_f32_16x16x32_f16 v[22:25], v[134:137], v[228:231], v[22:25]
	v_mfma_f32_16x16x32_f16 v[18:21], v[142:145], v[228:231], v[18:21]
	s_setprio 0
	s_setprio 1
	v_mfma_f32_16x16x32_f16 v[46:49], v[146:149], v[200:203], v[46:49]
	v_mfma_f32_16x16x32_f16 v[42:45], v[154:157], v[200:203], v[42:45]
	v_mfma_f32_16x16x32_f16 v[30:33], v[146:149], v[208:211], v[30:33]
	v_mfma_f32_16x16x32_f16 v[26:29], v[154:157], v[208:211], v[26:29]
	v_mfma_f32_16x16x32_f16 v[14:17], v[146:149], v[216:219], v[14:17]
	v_mfma_f32_16x16x32_f16 v[10:13], v[154:157], v[216:219], v[10:13]
	v_mfma_f32_16x16x32_f16 v[6:9], v[146:149], v[224:227], v[6:9]
	v_mfma_f32_16x16x32_f16 v[2:5], v[154:157], v[224:227], v[2:5]
	v_mfma_f32_16x16x32_f16 v[46:49], v[150:153], v[204:207], v[46:49]
	v_mfma_f32_16x16x32_f16 v[42:45], v[158:161], v[204:207], v[42:45]
	v_mfma_f32_16x16x32_f16 v[30:33], v[150:153], v[212:215], v[30:33]
	v_mfma_f32_16x16x32_f16 v[26:29], v[158:161], v[212:215], v[26:29]
	v_mfma_f32_16x16x32_f16 v[14:17], v[150:153], v[220:223], v[14:17]
	v_mfma_f32_16x16x32_f16 v[10:13], v[158:161], v[220:223], v[10:13]
	v_mfma_f32_16x16x32_f16 v[6:9], v[150:153], v[228:231], v[6:9]
	v_mfma_f32_16x16x32_f16 v[2:5], v[158:161], v[228:231], v[2:5]
	s_add_i32 s56, s56, 2
	s_add_u32 s6, s6, 0x100
	s_addc_u32 s7, s7, 0
	s_add_u32 s54, s54, 0x100
	s_addc_u32 s55, s55, 0
	s_setprio 0
	s_barrier
	s_cmp_gt_u32 s56, 29
	s_cbranch_scc0 .LBB1_9
	s_and_b64 vcc, exec, s[46:47]
	s_cbranch_vccz .LBB1_12
	s_barrier

.LBB1_15:
	v_readfirstlane_b32 s86, v172
	v_readfirstlane_b32 s87, v173
	v_readfirstlane_b32 s88, v174
	v_readfirstlane_b32 s89, v175
	v_lshrrev_b32_e32 v232, 3, v198
	v_and_b32_e32 v233, 7, v198
	v_xor_b32_e32 v233, v233, v232
	s_and_b32 s84, s27, 0x7ff
	s_lshr_b32 s85, s62, 1
	s_lshl_b32 s85, s85, 7
	s_add_i32 s84, s84, s85
	s_and_b32 s85, s62, 1
	s_lshl_b32 s85, s85, 5
	s_add_i32 s84, s84, s85
	v_add_u32_e32 v232, s84, v232
	v_lshlrev_b32_e32 v232, 7, v232
	v_lshl_add_u32 v232, v233, 4, v232
	s_bfe_u32 s91, s27, 0x10006
	s_lshl_b32 s90, s91, 2
	s_add_i32 s90, s90, s62
	s_lshl_b32 s90, s90, 10
	s_add_u32 s92, s86, 0x0
	s_addc_u32 s93, s87, 0
	s_add_i32 m0, s90, 0x0
	s_nop 0
	global_load_lds_dwordx4 v232, s[92:93]
	s_add_u32 s92, s86, 0x400
	s_addc_u32 s93, s87, 0
	s_add_i32 m0, s90, 0x2000
	s_nop 0
	global_load_lds_dwordx4 v232, s[92:93]
	s_add_u32 s92, s86, 0x800
	s_addc_u32 s93, s87, 0
	s_add_i32 m0, s90, 0x4000
	s_nop 0
	global_load_lds_dwordx4 v232, s[92:93]
	s_add_u32 s92, s86, 0xc00
	s_addc_u32 s93, s87, 0
	s_add_i32 m0, s90, 0x6000
	s_nop 0
	global_load_lds_dwordx4 v232, s[92:93]
	s_add_u32 s92, s88, 0x0
	s_addc_u32 s93, s89, 0
	s_add_i32 m0, s90, 0x8000
	s_nop 0
	global_load_lds_dwordx4 v232, s[92:93]
	s_add_u32 s92, s88, 0x400
	s_addc_u32 s93, s89, 0
	s_add_i32 m0, s90, 0xa000
	s_nop 0
	global_load_lds_dwordx4 v232, s[92:93]
	s_add_u32 s92, s88, 0x800
	s_addc_u32 s93, s89, 0
	s_add_i32 m0, s90, 0xc000
	s_nop 0
	global_load_lds_dwordx4 v232, s[92:93]
	s_add_u32 s92, s88, 0xc00
	s_addc_u32 s93, s89, 0
	s_add_i32 m0, s90, 0xe000
	s_nop 0
	global_load_lds_dwordx4 v232, s[92:93]
	v_and_b32_e32 v234, 15, v198
	v_lshrrev_b32_e32 v235, 4, v198
	v_and_b32_e32 v236, 7, v234
	v_lshrrev_b32_e32 v237, 3, v234
	v_lshlrev_b32_e32 v238, 1, v235
	v_xor_b32_e32 v239, v238, v236
	v_or_b32_e32 v238, 1, v238
	v_xor_b32_e32 v238, v238, v236
	v_lshlrev_b32_e32 v237, 13, v237
	v_lshl_add_u32 v237, v236, 7, v237
	s_lshl_b32 s91, s91, 12
	v_add_u32_e32 v237, s91, v237
	v_lshl_add_u32 v244, v239, 4, v237
	v_lshl_add_u32 v245, v238, 4, v237
	s_cmp_gt_i32 s77, 7
	s_cselect_b64 s[52:53], -1, 0
	s_lshl_b32 s4, s77, 2
	s_add_i32 s78, s4, s66
	s_or_b32 s37, s4, s62
	s_lshr_b32 s4, s27, 8
	s_and_b32 s4, s4, 0x7ff8
	v_and_b32_e32 v147, 64, v198
	s_add_i32 s10, s4, s78
	s_lshr_b32 s4, s27, 6
	v_xor_b32_e32 v146, 16, v198
	v_add_u32_e32 v206, 64, v147
	s_and_b32 s4, s4, 0x7fe0
	v_cmp_lt_i32_e32 vcc, v146, v206
	s_add_i32 s54, s4, s37
	s_cmp_lt_i32 s77, 8
	v_cndmask_b32_e32 v146, v198, v146, vcc
	v_lshlrev_b32_e32 v201, 2, v146
	v_mul_f32_e32 v146, v127, v127
	v_mul_f32_e32 v147, v129, v129
	s_cselect_b64 s[6:7], -1, 0
	v_fmac_f32_e32 v146, v126, v126
	v_fmac_f32_e32 v147, v128, v128
	s_and_b64 s[4:5], s[6:7], exec
	v_add_f32_e32 v153, v146, v147
	v_pk_mul_f32 v[146:147], v[124:125], v[124:125]
	v_pk_mul_f32 v[148:149], v[122:123], v[122:123]
	s_cselect_b32 s9, s23, s25
	s_cselect_b32 s8, s22, s24
	v_and_b32_e32 v152, 0x7cf, v199
	v_mov_b32_e32 v150, v146
	v_mov_b32_e32 v151, v148
	v_mov_b32_e32 v148, v147
	global_load_dwordx4 v[138:141], v194, s[8:9] offset:16
	global_load_dwordx4 v[142:145], v194, s[8:9]
	global_load_dwordx4 v[130:133], v194, s[8:9] offset:144
	global_load_dwordx4 v[134:137], v194, s[8:9] offset:128
	v_pk_add_f32 v[146:147], v[150:151], v[148:149]
	v_lshlrev_b32_e32 v170, 7, v152
	v_add_f32_e32 v147, v153, v147
	v_add_f32_e32 v207, v146, v147
	s_nop 0
	s_nop 0
	s_nop 0
	v_pk_mul_f32 v[184:185], v[112:113], v[112:113]
	v_pk_mul_f32 v[202:203], v[110:111], v[110:111]
	v_mov_b32_e32 v204, v184
	v_mov_b32_e32 v205, v202
	v_mov_b32_e32 v202, v185
	v_pk_add_f32 v[184:185], v[204:205], v[202:203]
	v_pk_mul_f32 v[202:203], v[106:107], v[106:107]
	v_add_f32_e32 v170, v207, v185
	v_add_f32_e32 v170, v184, v170
	v_pk_mul_f32 v[184:185], v[108:109], v[108:109]
	v_mov_b32_e32 v205, v202
	v_mov_b32_e32 v204, v184
	v_mov_b32_e32 v202, v185
	v_pk_add_f32 v[184:185], v[204:205], v[202:203]
	v_cndmask_b32_e64 v200, 1.0, v197, s[6:7]
	v_add_f32_e32 v170, v185, v170
	v_add_f32_e32 v170, v184, v170
	v_mov_b32_e32 v184, v170
	s_nop 1
	v_permlane16_swap_b32_e32 v184, v170
	v_xor_b32_e32 v185, 32, v198
	v_cmp_lt_i32_e32 vcc, v185, v206
	s_cselect_b32 s55, s17, s19
	v_or_b32_e32 v229, 16, v199
	v_cndmask_b32_e32 v185, v198, v185, vcc
	v_lshlrev_b32_e32 v202, 2, v185
	s_waitcnt lgkmcnt(0)
	v_add_f32_e32 v170, v170, v184
	v_mov_b32_e32 v184, v170
	s_nop 1
	v_permlane32_swap_b32_e32 v184, v170
	s_waitcnt lgkmcnt(0)
	v_add_f32_e32 v170, v170, v184
	v_fmamk_f32 v170, v170, 0x3c800000, v195
	v_mul_f32_e32 v184, 0x4f800000, v170
	v_cmp_gt_f32_e32 vcc, s70, v170
	s_nop 1
	v_cndmask_b32_e32 v170, v170, v184, vcc
	v_sqrt_f32_e32 v184, v170
	s_nop 0
	v_add_u32_e32 v185, -1, v184
	v_fma_f32 v203, -v185, v184, v170
	v_cmp_ge_f32_e64 s[8:9], 0, v203
	v_add_u32_e32 v203, 1, v184
	s_nop 0
	v_cndmask_b32_e64 v185, v184, v185, s[8:9]
	v_fma_f32 v184, -v203, v184, v170
	v_cmp_lt_f32_e64 s[8:9], 0, v184
	s_nop 1
	v_cndmask_b32_e64 v184, v185, v203, s[8:9]
	v_mul_f32_e32 v185, 0x37800000, v184
	v_cndmask_b32_e32 v184, v184, v185, vcc
	v_cmp_class_f32_e32 vcc, v170, v196
	v_lshl_or_b32 v203, s10, 17, v187
	v_lshl_or_b32 v185, s54, 17, v188
	v_cndmask_b32_e32 v170, v184, v170, vcc
	v_div_scale_f32 v184, s[8:9], v170, v170, v200
	v_rcp_f32_e32 v204, v184
	s_cselect_b32 s54, s16, s18
	s_cselect_b32 s10, s72, 0x1000
	v_fma_f32 v205, -v184, v204, 1.0
	v_fmac_f32_e32 v204, v205, v204
	v_div_scale_f32 v205, vcc, v200, v170, v200
	v_mul_f32_e32 v206, v205, v204
	v_fma_f32 v207, -v184, v206, v205
	v_fmac_f32_e32 v206, v207, v204
	v_fma_f32 v184, -v184, v206, v205
	v_div_fmas_f32 v184, v184, v204, v206
	v_div_fixup_f32 v170, v184, v170, v200
	v_pk_mul_f32 v[216:217], v[106:107], v[170:171] op_sel_hi:[1,0]
	v_pk_mul_f32 v[210:211], v[122:123], v[170:171] op_sel_hi:[1,0]
	s_waitcnt vmcnt(0)
	s_barrier
	ds_read_b128 v[146:149], v245 offset:32768
	ds_read_b128 v[150:153], v244 offset:32768
	ds_read_b128 v[154:157], v245 offset:0
	ds_read_b128 v[158:161], v244 offset:0
	s_waitcnt lgkmcnt(0)
	v_pk_mul_f32 v[216:217], v[130:131], v[216:217]
	v_pk_mul_f32 v[210:211], v[138:139], v[210:211]
	v_pk_mul_f32 v[224:225], v[146:147], v[216:217]
	v_pk_mul_f32 v[212:213], v[110:111], v[170:171] op_sel_hi:[1,0]
	v_pk_fma_f32 v[224:225], v[154:155], v[210:211], v[224:225] neg_lo:[0,0,1] neg_hi:[0,0,1]
	v_pk_mul_f32 v[154:155], v[154:155], v[216:217]
	v_pk_mul_f32 v[214:215], v[112:113], v[170:171] op_sel_hi:[1,0]
	v_pk_mul_f32 v[218:219], v[108:109], v[170:171] op_sel_hi:[1,0]
	v_pk_fma_f32 v[154:155], v[146:147], v[210:211], v[154:155]
	v_lshlrev_b32_e32 v146, 6, v199
	v_pk_mul_f32 v[204:205], v[128:129], v[170:171] op_sel_hi:[1,0]
	v_pk_mul_f32 v[206:207], v[126:127], v[170:171] op_sel_hi:[1,0]
	v_pk_mul_f32 v[208:209], v[124:125], v[170:171] op_sel_hi:[1,0]
	v_pk_mul_f32 v[214:215], v[136:137], v[214:215]
	v_pk_mul_f32 v[212:213], v[134:135], v[212:213]
	v_pk_mul_f32 v[218:219], v[132:133], v[218:219]
	v_cndmask_b32_e64 v184, v203, v185, s[6:7]
	v_and_b32_e32 v228, 0x1f000, v146
	v_pk_mul_f32 v[206:207], v[142:143], v[206:207]
	v_pk_mul_f32 v[204:205], v[144:145], v[204:205]
	v_pk_mul_f32 v[208:209], v[140:141], v[208:209]
	v_pk_mul_f32 v[220:221], v[150:151], v[212:213]
	v_pk_mul_f32 v[222:223], v[152:153], v[214:215]
	v_pk_mul_f32 v[226:227], v[148:149], v[218:219]
	v_or3_b32 v146, v228, v189, v184
	v_pk_fma_f32 v[222:223], v[160:161], v[204:205], v[222:223] neg_lo:[0,0,1] neg_hi:[0,0,1]
	v_pk_fma_f32 v[220:221], v[158:159], v[206:207], v[220:221] neg_lo:[0,0,1] neg_hi:[0,0,1]
	v_pk_fma_f32 v[226:227], v[156:157], v[208:209], v[226:227] neg_lo:[0,0,1] neg_hi:[0,0,1]
	v_pk_mul_f32 v[158:159], v[158:159], v[212:213]
	v_pk_mul_f32 v[160:161], v[160:161], v[214:215]
	v_pk_mul_f32 v[156:157], v[156:157], v[218:219]
	v_ashrrev_i32_e32 v147, 31, v146
	v_pk_fma_f32 v[152:153], v[152:153], v[204:205], v[160:161]
	v_pk_fma_f32 v[150:151], v[150:151], v[206:207], v[158:159]
	v_pk_fma_f32 v[156:157], v[148:149], v[208:209], v[156:157]
	v_lshl_add_u64 v[158:159], v[146:147], 1, s[54:55]
	v_cvt_pk_f16_f32 v146, v220, v221
	v_cvt_pk_f16_f32 v147, v222, v223
	v_cvt_pk_f16_f32 v148, v224, v225
	v_cvt_pk_f16_f32 v149, v226, v227
	v_cvt_pk_f16_f32 v150, v150, v151
	v_cvt_pk_f16_f32 v151, v152, v153
	v_cvt_pk_f16_f32 v152, v154, v155
	v_cvt_pk_f16_f32 v153, v156, v157
	global_store_dwordx4 v[158:159], v[146:149], off sc1
	v_pk_mul_f32 v[204:205], v[96:97], v[96:97]
	v_pk_mul_f32 v[206:207], v[94:95], v[94:95]
	v_lshl_add_u64 v[146:147], v[158:159], 0, s[10:11]
	global_store_dwordx4 v[146:147], v[150:153], off sc1
	v_mul_f32_e32 v146, v119, v119
	v_mul_f32_e32 v147, v121, v121
	v_fmac_f32_e32 v146, v118, v118
	v_fmac_f32_e32 v147, v120, v120
	v_add_f32_e32 v153, v146, v147
	v_pk_mul_f32 v[146:147], v[116:117], v[116:117]
	v_pk_mul_f32 v[148:149], v[114:115], v[114:115]
	v_bitop3_b32 v152, v199, s73, 16 bitop3:0xc8
	v_mov_b32_e32 v150, v146
	v_mov_b32_e32 v151, v148
	v_mov_b32_e32 v148, v147
	v_pk_add_f32 v[146:147], v[150:151], v[148:149]
	v_lshlrev_b32_e32 v170, 7, v152
	v_add_f32_e32 v147, v153, v147
	v_add_f32_e32 v210, v146, v147
	ds_read_b128 v[146:149], v245 offset:49152
	s_nop 0
	ds_read_b128 v[150:153], v244 offset:49152
	s_nop 0
	ds_read_b128 v[154:157], v245 offset:16384
	s_nop 0
	ds_read_b128 v[158:161], v244 offset:16384
	v_mov_b32_e32 v208, v204
	v_mov_b32_e32 v209, v206
	v_mov_b32_e32 v206, v205
	v_pk_add_f32 v[204:205], v[208:209], v[206:207]
	v_pk_mul_f32 v[206:207], v[90:91], v[90:91]
	v_add_f32_e32 v170, v210, v205
	v_add_f32_e32 v170, v204, v170
	v_pk_mul_f32 v[204:205], v[92:93], v[92:93]
	v_mov_b32_e32 v209, v206
	v_mov_b32_e32 v208, v204
	v_mov_b32_e32 v206, v205
	v_pk_add_f32 v[204:205], v[208:209], v[206:207]
	s_nop 0
	v_add_f32_e32 v170, v205, v170
	v_add_f32_e32 v170, v204, v170
	v_mov_b32_e32 v204, v170
	s_nop 1
	v_permlane16_swap_b32_e32 v204, v170
	s_waitcnt lgkmcnt(0)
	v_add_f32_e32 v170, v170, v204
	v_mov_b32_e32 v204, v170
	s_nop 1
	v_permlane32_swap_b32_e32 v204, v170
	s_waitcnt lgkmcnt(0)
	v_add_f32_e32 v170, v170, v204
	v_fmamk_f32 v170, v170, 0x3c800000, v195
	v_mul_f32_e32 v204, 0x4f800000, v170
	v_cmp_gt_f32_e32 vcc, s70, v170
	s_nop 1
	v_cndmask_b32_e32 v170, v170, v204, vcc
	v_sqrt_f32_e32 v204, v170
	s_nop 0
	v_add_u32_e32 v205, -1, v204
	v_fma_f32 v206, -v205, v204, v170
	v_cmp_ge_f32_e64 s[8:9], 0, v206
	v_add_u32_e32 v206, 1, v204
	s_nop 0
	v_cndmask_b32_e64 v205, v204, v205, s[8:9]
	v_fma_f32 v204, -v206, v204, v170
	v_cmp_lt_f32_e64 s[8:9], 0, v204
	s_nop 1
	v_cndmask_b32_e64 v204, v205, v206, s[8:9]
	v_mul_f32_e32 v205, 0x37800000, v204
	v_cndmask_b32_e32 v204, v204, v205, vcc
	v_cmp_class_f32_e32 vcc, v170, v196
	s_nop 1
	v_cndmask_b32_e32 v170, v204, v170, vcc
	v_div_scale_f32 v204, s[8:9], v170, v170, v200
	v_rcp_f32_e32 v205, v204
	s_mov_b64 s[8:9], -1
	v_fma_f32 v206, -v204, v205, 1.0
	v_fmac_f32_e32 v205, v206, v205
	v_div_scale_f32 v206, vcc, v200, v170, v200
	v_mul_f32_e32 v207, v206, v205
	v_fma_f32 v208, -v204, v207, v206
	v_fmac_f32_e32 v207, v208, v205
	v_fma_f32 v204, -v204, v207, v206
	v_div_fmas_f32 v204, v204, v205, v207
	v_div_fixup_f32 v170, v204, v170, v200
	v_pk_mul_f32 v[216:217], v[90:91], v[170:171] op_sel_hi:[1,0]
	v_pk_mul_f32 v[210:211], v[114:115], v[170:171] op_sel_hi:[1,0]
	v_pk_mul_f32 v[216:217], v[130:131], v[216:217]
	v_pk_mul_f32 v[210:211], v[138:139], v[210:211]
	v_pk_mul_f32 v[212:213], v[94:95], v[170:171] op_sel_hi:[1,0]
	v_pk_mul_f32 v[214:215], v[96:97], v[170:171] op_sel_hi:[1,0]
	s_waitcnt lgkmcnt(0)
	v_pk_mul_f32 v[224:225], v[146:147], v[216:217]
	v_pk_mul_f32 v[218:219], v[92:93], v[170:171] op_sel_hi:[1,0]
	s_waitcnt lgkmcnt(0)
	v_pk_fma_f32 v[224:225], v[154:155], v[210:211], v[224:225] neg_lo:[0,0,1] neg_hi:[0,0,1]
	v_pk_mul_f32 v[154:155], v[154:155], v[216:217]
	v_pk_mul_f32 v[204:205], v[120:121], v[170:171] op_sel_hi:[1,0]
	v_pk_fma_f32 v[154:155], v[146:147], v[210:211], v[154:155]
	v_lshlrev_b32_e32 v146, 3, v229
	v_pk_mul_f32 v[206:207], v[118:119], v[170:171] op_sel_hi:[1,0]
	v_pk_mul_f32 v[208:209], v[116:117], v[170:171] op_sel_hi:[1,0]
	v_pk_mul_f32 v[214:215], v[136:137], v[214:215]
	v_pk_mul_f32 v[212:213], v[134:135], v[212:213]
	v_pk_mul_f32 v[218:219], v[132:133], v[218:219]
	v_and_b32_e32 v146, 0xf8, v146
	v_pk_mul_f32 v[206:207], v[142:143], v[206:207]
	v_pk_mul_f32 v[204:205], v[144:145], v[204:205]
	v_pk_mul_f32 v[208:209], v[140:141], v[208:209]
	v_pk_mul_f32 v[220:221], v[150:151], v[212:213]
	v_pk_mul_f32 v[222:223], v[152:153], v[214:215]
	v_pk_mul_f32 v[226:227], v[148:149], v[218:219]
	v_or3_b32 v146, v228, v146, v184
	s_waitcnt lgkmcnt(0)
	v_pk_fma_f32 v[222:223], v[160:161], v[204:205], v[222:223] neg_lo:[0,0,1] neg_hi:[0,0,1]
	v_pk_fma_f32 v[220:221], v[158:159], v[206:207], v[220:221] neg_lo:[0,0,1] neg_hi:[0,0,1]
	v_pk_fma_f32 v[226:227], v[156:157], v[208:209], v[226:227] neg_lo:[0,0,1] neg_hi:[0,0,1]
	v_pk_mul_f32 v[158:159], v[158:159], v[212:213]
	v_pk_mul_f32 v[160:161], v[160:161], v[214:215]
	v_pk_mul_f32 v[156:157], v[156:157], v[218:219]
	v_ashrrev_i32_e32 v147, 31, v146
	v_pk_fma_f32 v[152:153], v[152:153], v[204:205], v[160:161]
	v_pk_fma_f32 v[150:151], v[150:151], v[206:207], v[158:159]
	v_pk_fma_f32 v[156:157], v[148:149], v[208:209], v[156:157]
	v_lshl_add_u64 v[158:159], v[146:147], 1, s[54:55]
	v_cvt_pk_f16_f32 v146, v220, v221
	v_cvt_pk_f16_f32 v147, v222, v223
	v_cvt_pk_f16_f32 v148, v224, v225
	v_cvt_pk_f16_f32 v149, v226, v227
	v_bitop3_b32 v184, v199, s74, 32 bitop3:0xc8
	v_cvt_pk_f16_f32 v150, v150, v151
	v_cvt_pk_f16_f32 v151, v152, v153
	v_cvt_pk_f16_f32 v152, v154, v155
	v_cvt_pk_f16_f32 v153, v156, v157
	global_store_dwordx4 v[158:159], v[146:149], off sc1
	v_lshlrev_b32_e32 v170, 7, v184
	v_mul_f32_e32 v204, v105, v105
	v_lshl_add_u64 v[146:147], v[158:159], 0, s[10:11]
	global_store_dwordx4 v[146:147], v[150:153], off sc1
	v_fmac_f32_e32 v204, v104, v104
	ds_read_b128 v[146:149], v245 offset:1024
	ds_read_b128 v[154:157], v244 offset:1024
	s_nop 0
	ds_read_b128 v[150:153], v245 offset:33792
	s_nop 0
	ds_read_b128 v[158:161], v244 offset:33792
	v_mul_f32_e32 v170, v103, v103
	v_fmac_f32_e32 v170, v102, v102
	v_add_f32_e32 v170, v170, v204
	v_pk_mul_f32 v[204:205], v[100:101], v[100:101]
	v_pk_mul_f32 v[206:207], v[98:99], v[98:99]
	v_mov_b32_e32 v208, v204
	v_mov_b32_e32 v209, v206
	v_mov_b32_e32 v206, v205
	v_pk_add_f32 v[204:205], v[208:209], v[206:207]
	v_pk_mul_f32 v[206:207], v[78:79], v[78:79]
	v_add_f32_e32 v170, v170, v205
	v_add_f32_e32 v170, v204, v170
	v_pk_mul_f32 v[204:205], v[80:81], v[80:81]
	v_mov_b32_e32 v209, v206
	v_mov_b32_e32 v208, v204
	v_mov_b32_e32 v206, v205
	v_pk_add_f32 v[204:205], v[208:209], v[206:207]
	v_pk_mul_f32 v[206:207], v[74:75], v[74:75]
	v_add_f32_e32 v170, v170, v205
	v_add_f32_e32 v170, v204, v170
	v_pk_mul_f32 v[204:205], v[76:77], v[76:77]
	v_mov_b32_e32 v209, v206
	v_mov_b32_e32 v208, v204
	v_mov_b32_e32 v206, v205
	v_pk_add_f32 v[204:205], v[208:209], v[206:207]
	s_mov_b64 vcc, s[4:5]
	v_add_f32_e32 v170, v205, v170
	v_add_f32_e32 v170, v204, v170
	v_mov_b32_e32 v204, v170
	s_nop 1
	v_permlane16_swap_b32_e32 v204, v170
	v_lshlrev_b32_e32 v205, 6, v184
	s_waitcnt lgkmcnt(0)
	v_add_f32_e32 v170, v170, v204
	v_mov_b32_e32 v204, v170
	s_nop 1
	v_permlane32_swap_b32_e32 v204, v170
	s_cbranch_vccnz .LBB1_17
	v_or_b32_e32 v184, 32, v199
	v_lshlrev_b32_e32 v184, 3, v184
	v_and_b32_e32 v206, 0x1f000, v205
	v_and_b32_e32 v184, 0x178, v184
	v_or3_b32 v184, v206, v184, v203
	s_mov_b64 s[8:9], 0

.LBB3_24:
	s_waitcnt lgkmcnt(14)
	v_mfma_f32_32x32x16_f16 v[34:49], v[174:177], v[186:189], v[34:49]
	v_exp_f32_e32 v98, v98
	v_exp_f32_e32 v99, v99
	v_exp_f32_e32 v100, v100
	v_exp_f32_e32 v101, v101
	s_waitcnt lgkmcnt(12)
	v_mfma_f32_32x32x16_f16 v[50:65], v[174:177], v[182:185], v[50:65]
	v_exp_f32_e32 v102, v102
	v_exp_f32_e32 v103, v103
	v_exp_f32_e32 v104, v104
	v_exp_f32_e32 v105, v105
	v_add_u32_e32 v3, s58, v230
	ds_read_b128 v[206:209], v3
	ds_read_b128 v[202:205], v3 offset:512
	s_waitcnt lgkmcnt(12)
	v_mfma_f32_32x32x16_f16 v[34:49], v[170:173], v[178:181], v[34:49]
	v_exp_f32_e32 v106, v106
	v_exp_f32_e32 v107, v107
	v_exp_f32_e32 v108, v108
	v_exp_f32_e32 v109, v109
	ds_read_b128 v[198:201], v3 offset:2048
	ds_read_b128 v[194:197], v3 offset:2560
	s_waitcnt lgkmcnt(12)
	v_mfma_f32_32x32x16_f16 v[50:65], v[170:173], v[134:137], v[50:65]
	v_exp_f32_e32 v110, v110
	v_exp_f32_e32 v111, v111
	v_exp_f32_e32 v112, v112
	v_exp_f32_e32 v113, v113
	ds_read_b128 v[190:193], v3 offset:4096
	ds_read_b128 v[186:189], v3 offset:4608
	s_waitcnt lgkmcnt(12)
	v_mfma_f32_32x32x16_f16 v[34:49], v[166:169], v[130:133], v[34:49]
	v_exp_f32_e32 v82, v82
	v_exp_f32_e32 v83, v83
	v_exp_f32_e32 v84, v84
	v_exp_f32_e32 v85, v85
	ds_read_b128 v[182:185], v3 offset:6144
	ds_read_b128 v[178:181], v3 offset:6656
	s_waitcnt lgkmcnt(12)
	v_mfma_f32_32x32x16_f16 v[50:65], v[166:169], v[12:15], v[50:65]
	v_exp_f32_e32 v86, v86
	v_exp_f32_e32 v87, v87
	v_exp_f32_e32 v88, v88
	v_exp_f32_e32 v89, v89
	s_waitcnt lgkmcnt(10)
	v_mfma_f32_32x32x16_f16 v[34:49], v[158:161], v[8:11], v[34:49]
	v_exp_f32_e32 v90, v90
	v_exp_f32_e32 v91, v91
	v_exp_f32_e32 v92, v92
	v_exp_f32_e32 v93, v93
	s_waitcnt lgkmcnt(8)
	v_mfma_f32_32x32x16_f16 v[50:65], v[158:161], v[4:7], v[50:65]
	v_exp_f32_e32 v94, v94
	v_exp_f32_e32 v95, v95
	v_exp_f32_e32 v96, v96
	v_exp_f32_e32 v97, v97
	s_add_i32 s16, s37, 2
	s_add_i32 s62, s58, 0x2000
	s_cmpk_lg_i32 s58, 0x4000
	s_cselect_b32 s60, s62, 0
	s_add_u32 s6, s6, 0x4000
	s_addc_u32 s7, s7, 0
	s_add_i32 s62, s37, 7
	v_add_u32_e32 v16, 16, v16
	s_waitcnt vmcnt(2) lgkmcnt(0)
	s_barrier
	s_andn2_b64 vcc, exec, s[28:29]
	s_cbranch_vccnz .LBB3_26
	s_waitcnt lgkmcnt(0)
	v_add_u32_e32 v3, s55, v232
	ds_read_b128 v[4:7], v3 offset:49248
	ds_read_b128 v[8:11], v3 offset:49216
	ds_read_b128 v[12:15], v3 offset:49184
	ds_read_b128 v[114:117], v3 offset:49152
	s_waitcnt lgkmcnt(3)
	v_pk_mul_f32 v[46:47], v[46:47], v[4:5]
	s_waitcnt lgkmcnt(2)
	v_pk_mul_f32 v[42:43], v[42:43], v[8:9]
	s_waitcnt lgkmcnt(1)
	v_pk_mul_f32 v[38:39], v[38:39], v[12:13]
	v_pk_mul_f32 v[48:49], v[48:49], v[6:7]
	v_pk_mul_f32 v[44:45], v[44:45], v[10:11]
	v_pk_mul_f32 v[40:41], v[40:41], v[14:15]
	s_waitcnt lgkmcnt(0)
	v_pk_mul_f32 v[36:37], v[36:37], v[116:117]
	v_pk_mul_f32 v[34:35], v[34:35], v[114:115]
	v_pk_mul_f32 v[62:63], v[62:63], v[4:5]
	v_pk_mul_f32 v[58:59], v[58:59], v[8:9]
	v_pk_mul_f32 v[54:55], v[54:55], v[12:13]
	v_pk_mul_f32 v[64:65], v[64:65], v[6:7]
	v_pk_mul_f32 v[60:61], v[60:61], v[10:11]
	v_pk_mul_f32 v[56:57], v[56:57], v[14:15]
	v_pk_mul_f32 v[52:53], v[52:53], v[116:117]
	v_pk_mul_f32 v[50:51], v[50:51], v[114:115]
.LBB3_26:
	s_cmp_ge_u32 s62, s59
	s_cbranch_scc1 .LBB3_35
	s_mov_b32 s34, s38
	s_mov_b32 s38, s60
	s_mov_b32 s37, s16
	s_branch .LBB3_12

	.amdhsa_kernel _Z11attn_kernelPKDF16_S0_S0_PDF16_PKjS3_
		.amdhsa_group_segment_fixed_size 0
		.amdhsa_private_segment_fixed_size 0
		.amdhsa_kernarg_size 48
		.amdhsa_user_sgpr_count 2
		.amdhsa_user_sgpr_dispatch_ptr 0
		.amdhsa_user_sgpr_queue_ptr 0
		.amdhsa_user_sgpr_kernarg_segment_ptr 1
		.amdhsa_user_sgpr_dispatch_id 0
		.amdhsa_user_sgpr_kernarg_preload_length 0
		.amdhsa_user_sgpr_kernarg_preload_offset 0
		.amdhsa_user_sgpr_private_segment_size 0
		.amdhsa_uses_dynamic_stack 0
		.amdhsa_enable_private_segment 0
		.amdhsa_system_sgpr_workgroup_id_x 1
		.amdhsa_system_sgpr_workgroup_id_y 0
		.amdhsa_system_sgpr_workgroup_id_z 0
		.amdhsa_system_sgpr_workgroup_info 0
		.amdhsa_system_vgpr_workitem_id 0
		.amdhsa_next_free_vgpr 248
		.amdhsa_next_free_sgpr 63
		.amdhsa_accum_offset 248
		.amdhsa_reserve_vcc 1
		.amdhsa_float_round_mode_32 0
		.amdhsa_float_round_mode_16_64 0
		.amdhsa_float_denorm_mode_32 3
		.amdhsa_float_denorm_mode_16_64 3
		.amdhsa_dx10_clamp 1
		.amdhsa_ieee_mode 1
		.amdhsa_fp16_overflow 0
		.amdhsa_tg_split 0
		.amdhsa_exception_fp_ieee_invalid_op 0
		.amdhsa_exception_fp_denorm_src 0
		.amdhsa_exception_fp_ieee_div_zero 0
		.amdhsa_exception_fp_ieee_overflow 0
		.amdhsa_exception_fp_ieee_underflow 0
		.amdhsa_exception_fp_ieee_inexact 0
		.amdhsa_exception_int_div_zero 0
	.end_amdhsa_kernel

amdhsa.kernels:
  - .agpr_count:     0
    .args:
      - .actual_access:  read_only
        .address_space:  global
        .offset:         0
        .size:           8
        .value_kind:     global_buffer
      - .actual_access:  read_only
        .address_space:  global
        .offset:         8
        .size:           8
        .value_kind:     global_buffer
      - .actual_access:  read_only
        .address_space:  global
        .offset:         16
        .size:           8
        .value_kind:     global_buffer
      - .actual_access:  write_only
        .address_space:  global
        .offset:         24
        .size:           8
        .value_kind:     global_buffer
      - .actual_access:  write_only
        .address_space:  global
        .offset:         32
        .size:           8
        .value_kind:     global_buffer
      - .actual_access:  write_only
        .address_space:  global
        .offset:         40
        .size:           8
        .value_kind:     global_buffer
      - .actual_access:  write_only
        .address_space:  global
        .offset:         48
        .size:           8
        .value_kind:     global_buffer
    .group_segment_fixed_size: 0
    .kernarg_segment_align: 8
    .kernarg_segment_size: 56
    .language:       OpenCL C
    .language_version:
      - 2
      - 0
    .max_flat_workgroup_size: 1024
    .name:           _Z11prep_kernelPKfS0_PKiPDF16_S3_PfS4_
    .private_segment_fixed_size: 0
    .sgpr_count:     24
    .sgpr_spill_count: 0
    .symbol:         _Z11prep_kernelPKfS0_PKiPDF16_S3_PfS4_.kd
    .uniform_work_group_size: 1
    .uses_dynamic_stack: false
    .vgpr_count:     40
    .vgpr_spill_count: 0
    .wavefront_size: 64
  - .agpr_count:     0
    .args:
      - .address_space:  global
        .offset:         0
        .size:           8
        .value_kind:     global_buffer
      - .address_space:  global
        .offset:         8
        .size:           8
        .value_kind:     global_buffer
      - .address_space:  global
        .offset:         16
        .size:           8
        .value_kind:     global_buffer
      - .address_space:  global
        .offset:         24
        .size:           8
        .value_kind:     global_buffer
      - .address_space:  global
        .offset:         32
        .size:           8
        .value_kind:     global_buffer
      - .address_space:  global
        .offset:         40
        .size:           8
        .value_kind:     global_buffer
      - .address_space:  global
        .offset:         48
        .size:           8
        .value_kind:     global_buffer
      - .address_space:  global
        .offset:         56
        .size:           8
        .value_kind:     global_buffer
      - .address_space:  global
        .offset:         64
        .size:           8
        .value_kind:     global_buffer
      - .address_space:  global
        .offset:         72
        .size:           8
        .value_kind:     global_buffer
      - .address_space:  global
        .offset:         80
        .size:           8
        .value_kind:     global_buffer
      - .address_space:  global
        .offset:         88
        .size:           8
        .value_kind:     global_buffer
      - .address_space:  global
        .offset:         96
        .size:           8
        .value_kind:     global_buffer
      - .address_space:  global
        .offset:         104
        .size:           8
        .value_kind:     global_buffer
    .group_segment_fixed_size: 0
    .kernarg_segment_align: 8
    .kernarg_segment_size: 112
    .language:       OpenCL C
    .language_version:
      - 2
      - 0
    .max_flat_workgroup_size: 512
    .name:           _Z15gemm_qkv_kernelPKDF16_S0_PDF16_S1_S1_PKfS3_S3_S3_S3_S1_PKiPyPj
    .private_segment_fixed_size: 0
    .sgpr_count:     100
    .sgpr_spill_count: 0
    .symbol:         _Z15gemm_qkv_kernelPKDF16_S0_PDF16_S1_S1_PKfS3_S3_S3_S3_S1_PKiPyPj.kd
    .uniform_work_group_size: 1
    .uses_dynamic_stack: false
    .vgpr_count:     248
    .vgpr_spill_count: 0
    .wavefront_size: 64
  - .agpr_count:     0
    .args:
      - .address_space:  global
        .offset:         0
        .size:           8
        .value_kind:     global_buffer
      - .address_space:  global
        .offset:         8
        .size:           8
        .value_kind:     global_buffer
      - .address_space:  global
        .offset:         16
        .size:           8
        .value_kind:     global_buffer
    .group_segment_fixed_size: 0
    .kernarg_segment_align: 8
    .kernarg_segment_size: 24
    .language:       OpenCL C
    .language_version:
      - 2
      - 0
    .max_flat_workgroup_size: 512
    .name:           _Z15gemm_out_kernelPKDF16_S0_Pf
    .private_segment_fixed_size: 0
    .sgpr_count:     26
    .sgpr_spill_count: 0
    .symbol:         _Z15gemm_out_kernelPKDF16_S0_Pf.kd
    .uniform_work_group_size: 1
    .uses_dynamic_stack: false
    .vgpr_count:     148
    .vgpr_spill_count: 0
    .wavefront_size: 64
  - .agpr_count:     0
    .args:
      - .address_space:  global
        .offset:         0
        .size:           8
        .value_kind:     global_buffer
      - .address_space:  global
        .offset:         8
        .size:           8
        .value_kind:     global_buffer
      - .address_space:  global
        .offset:         16
        .size:           8
        .value_kind:     global_buffer
      - .address_space:  global
        .offset:         24
        .size:           8
        .value_kind:     global_buffer
      - .address_space:  global
        .offset:         32
        .size:           8
        .value_kind:     global_buffer
      - .address_space:  global
        .offset:         40
        .size:           8
        .value_kind:     global_buffer
    .group_segment_fixed_size: 0
    .kernarg_segment_align: 8
    .kernarg_segment_size: 48
    .language:       OpenCL C
    .language_version:
      - 2
      - 0
    .max_flat_workgroup_size: 512
    .name:           _Z11attn_kernelPKDF16_S0_S0_PDF16_PKjS3_
    .private_segment_fixed_size: 0
    .sgpr_count:     69
    .sgpr_spill_count: 0
    .symbol:         _Z11attn_kernelPKDF16_S0_S0_PDF16_PKjS3_.kd
    .uniform_work_group_size: 1
    .uses_dynamic_stack: false
    .vgpr_count:     248
    .vgpr_spill_count: 0
    .wavefront_size: 64
